# speedup vs baseline: 1.0185x; 1.0185x over previous
.Lscan_loop:
	v_exp_f32_e32 v98, v98
	v_exp_f32_e32 v99, v99
	v_mfma_f32_16x16x32_f16 v[80:83], v[72:75], v[24:27], v[80:83]
	ds_read_b128 v[60:63], v92 offset:34816
	ds_bpermute_b32 v90, v87, v85
	s_waitcnt lgkmcnt(2)
	v_exp_f32_e32 v100, v100
	v_exp_f32_e32 v101, v101
	v_mfma_f32_32x32x8_f16 v[114:129], v[32:33], v[28:29], 0
	ds_read_u16 v32, v9 offset:64
	ds_read_b128 v[64:67], v92 offset:35840
	v_fmac_f32_e32 v132, v98, v195
	v_exp_f32_e32 v102, v102
	v_fmac_f32_e32 v133, v99, v132
	v_exp_f32_e32 v103, v103
	v_fmac_f32_e32 v134, v100, v133
	v_cvt_pkrtz_f16_f32 v68, v132, v133
	v_exp_f32_e32 v104, v104
	v_fmac_f32_e32 v135, v101, v134
	v_pk_mul_f16 v68, v52, v68
	v_exp_f32_e32 v105, v105
	v_add_f32_e32 v84, v80, v81
	v_add_f32_e32 v91, v82, v83
	v_fmac_f32_e32 v136, v102, v135
	v_add_f32_e32 v84, v84, v91
	v_cvt_pkrtz_f16_f32 v69, v134, v135
	v_mfma_f32_32x32x16_f16 v[148:163], v[36:39], v[44:47], 0
	ds_read_b128 v[44:47], v92 offset:4096
	ds_bpermute_b32 v89, v86, v84
	v_exp_f32_e32 v106, v106
	v_fmac_f32_e32 v137, v103, v136
	v_pk_mul_f16 v69, v53, v69
	v_exp_f32_e32 v107, v107
	v_fmac_f32_e32 v138, v104, v137
	v_cvt_pkrtz_f16_f32 v70, v136, v137
	v_exp_f32_e32 v108, v108
	v_fmac_f32_e32 v139, v105, v138
	v_pk_mul_f16 v70, v54, v70
	v_exp_f32_e32 v109, v109
	v_mfma_f32_32x32x16_f16 v[180:195], v[36:39], v[48:51], 0
	ds_read_b128 v[36:39], v11 offset:512
	ds_read_b128 v[48:51], v92 offset:5120
	v_cvt_pkrtz_f16_f32 v71, v138, v139
	v_fmac_f32_e32 v172, v106, v139
	v_pk_mul_f16 v71, v55, v71
	v_exp_f32_e32 v110, v110
	v_fmac_f32_e32 v173, v107, v172
	v_mfma_f32_16x16x32_f16 v[76:79], v[68:71], v[20:23], 0
	v_cvt_pkrtz_f16_f32 v72, v172, v173
	v_exp_f32_e32 v111, v111
	v_fmac_f32_e32 v174, v108, v173
	v_pk_mul_f16 v72, v56, v72
	v_fmac_f32_e32 v175, v109, v174
	v_exp_f32_e32 v112, v112
	v_cvt_pkrtz_f16_f32 v73, v174, v175
	v_fmac_f32_e32 v176, v110, v175
	v_pk_mul_f16 v73, v57, v73
	v_fmac_f32_e32 v177, v111, v176
	v_exp_f32_e32 v113, v113
	v_cvt_pkrtz_f16_f32 v74, v176, v177
	v_fmac_f32_e32 v178, v112, v177
	v_pk_mul_f16 v74, v58, v74
	s_waitcnt lgkmcnt(2)
	v_add_f32_e32 v202, v85, v90
	v_fmac_f32_e32 v179, v113, v178
	v_add_f32_e32 v88, v84, v89
	v_cvt_pkrtz_f16_f32 v75, v178, v179
	v_pk_mul_f16 v75, v59, v75
	v_exp_f32_e32 v114, v114
	v_exp_f32_e32 v115, v115
	v_mfma_f32_16x16x32_f16 v[76:79], v[72:75], v[24:27], v[76:79]
	ds_read_b128 v[52:55], v92 offset:36864
	ds_bpermute_b32 v90, v87, v88
	s_waitcnt lgkmcnt(2)
	v_exp_f32_e32 v116, v116
	v_exp_f32_e32 v117, v117
	v_mfma_f32_32x32x8_f16 v[98:113], v[32:33], v[28:29], 0
	ds_read_u16 v32, v9 offset:96
	ds_read_b128 v[56:59], v92 offset:37888
	v_fmac_f32_e32 v148, v114, v179
	v_exp_f32_e32 v118, v118
	v_fmac_f32_e32 v149, v115, v148
	v_exp_f32_e32 v119, v119
	v_fmac_f32_e32 v150, v116, v149
	v_cvt_pkrtz_f16_f32 v68, v148, v149
	v_exp_f32_e32 v120, v120
	v_fmac_f32_e32 v151, v117, v150
	v_pk_mul_f16 v68, v60, v68
	v_exp_f32_e32 v121, v121
	v_add_f32_e32 v84, v76, v77
	v_add_f32_e32 v91, v78, v79
	v_fmac_f32_e32 v152, v118, v151
	v_add_f32_e32 v84, v84, v91
	v_cvt_pkrtz_f16_f32 v69, v150, v151
	v_mfma_f32_32x32x16_f16 v[132:147], v[36:39], v[44:47], 0
	ds_read_b128 v[44:47], v92 offset:6144
	ds_bpermute_b32 v89, v86, v84
	v_exp_f32_e32 v122, v122
	v_fmac_f32_e32 v153, v119, v152
	v_pk_mul_f16 v69, v61, v69
	v_exp_f32_e32 v123, v123
	v_fmac_f32_e32 v154, v120, v153
	v_cvt_pkrtz_f16_f32 v70, v152, v153
	v_exp_f32_e32 v124, v124
	v_fmac_f32_e32 v155, v121, v154
	v_pk_mul_f16 v70, v62, v70
	v_exp_f32_e32 v125, v125
	v_mfma_f32_32x32x16_f16 v[164:179], v[36:39], v[48:51], 0
	ds_read_b128 v[36:39], v11 offset:768
	ds_read_b128 v[48:51], v92 offset:7168
	v_cvt_pkrtz_f16_f32 v71, v154, v155
	v_fmac_f32_e32 v188, v122, v155
	v_pk_mul_f16 v71, v63, v71
	v_exp_f32_e32 v126, v126
	v_fmac_f32_e32 v189, v123, v188
	v_mfma_f32_16x16x32_f16 v[80:83], v[68:71], v[20:23], 0
	v_cvt_pkrtz_f16_f32 v72, v188, v189
	v_exp_f32_e32 v127, v127
	v_fmac_f32_e32 v190, v124, v189
	v_pk_mul_f16 v72, v64, v72
	v_fmac_f32_e32 v191, v125, v190
	v_exp_f32_e32 v128, v128
	v_cvt_pkrtz_f16_f32 v73, v190, v191
	v_fmac_f32_e32 v192, v126, v191
	v_pk_mul_f16 v73, v65, v73
	v_fmac_f32_e32 v193, v127, v192
	v_exp_f32_e32 v129, v129
	v_cvt_pkrtz_f16_f32 v74, v192, v193
	v_fmac_f32_e32 v194, v128, v193
	v_pk_mul_f16 v74, v66, v74
	s_waitcnt lgkmcnt(2)
	v_add_f32_e32 v203, v88, v90
	v_fmac_f32_e32 v195, v129, v194
	v_add_f32_e32 v85, v84, v89
	v_cvt_pkrtz_f16_f32 v75, v194, v195
	v_pk_mul_f16 v75, v67, v75
	v_exp_f32_e32 v98, v98
	v_exp_f32_e32 v99, v99
	v_mfma_f32_16x16x32_f16 v[80:83], v[72:75], v[24:27], v[80:83]
	ds_read_b128 v[60:63], v92 offset:38912
	ds_bpermute_b32 v90, v87, v85
	s_waitcnt lgkmcnt(2)
	v_exp_f32_e32 v100, v100
	v_exp_f32_e32 v101, v101
	v_mfma_f32_32x32x8_f16 v[114:129], v[32:33], v[28:29], 0
	ds_read_u16 v32, v9 offset:128
	ds_read_b128 v[64:67], v92 offset:39936
	v_fmac_f32_e32 v132, v98, v195
	v_exp_f32_e32 v102, v102
	v_fmac_f32_e32 v133, v99, v132
	v_exp_f32_e32 v103, v103
	v_fmac_f32_e32 v134, v100, v133
	v_cvt_pkrtz_f16_f32 v68, v132, v133
	v_exp_f32_e32 v104, v104
	v_fmac_f32_e32 v135, v101, v134
	v_pk_mul_f16 v68, v52, v68
	v_exp_f32_e32 v105, v105
	v_add_f32_e32 v84, v80, v81
	v_add_f32_e32 v91, v82, v83
	v_fmac_f32_e32 v136, v102, v135
	v_add_f32_e32 v84, v84, v91
	v_cvt_pkrtz_f16_f32 v69, v134, v135
	v_mfma_f32_32x32x16_f16 v[148:163], v[36:39], v[44:47], 0
	ds_read_b128 v[44:47], v92 offset:8192
	ds_bpermute_b32 v89, v86, v84
	v_exp_f32_e32 v106, v106
	v_fmac_f32_e32 v137, v103, v136
	v_pk_mul_f16 v69, v53, v69
	v_exp_f32_e32 v107, v107
	v_fmac_f32_e32 v138, v104, v137
	v_cvt_pkrtz_f16_f32 v70, v136, v137
	v_exp_f32_e32 v108, v108
	v_fmac_f32_e32 v139, v105, v138
	v_pk_mul_f16 v70, v54, v70
	v_exp_f32_e32 v109, v109
	v_mfma_f32_32x32x16_f16 v[180:195], v[36:39], v[48:51], 0
	ds_read_b128 v[36:39], v11 offset:1024
	ds_read_b128 v[48:51], v92 offset:9216
	v_cvt_pkrtz_f16_f32 v71, v138, v139
	v_fmac_f32_e32 v172, v106, v139
	v_pk_mul_f16 v71, v55, v71
	v_exp_f32_e32 v110, v110
	v_fmac_f32_e32 v173, v107, v172
	v_mfma_f32_16x16x32_f16 v[76:79], v[68:71], v[20:23], 0
	v_cvt_pkrtz_f16_f32 v72, v172, v173
	v_exp_f32_e32 v111, v111
	v_fmac_f32_e32 v174, v108, v173
	v_pk_mul_f16 v72, v56, v72
	v_fmac_f32_e32 v175, v109, v174
	v_exp_f32_e32 v112, v112
	v_cvt_pkrtz_f16_f32 v73, v174, v175
	v_fmac_f32_e32 v176, v110, v175
	v_pk_mul_f16 v73, v57, v73
	v_fmac_f32_e32 v177, v111, v176
	v_exp_f32_e32 v113, v113
	v_cvt_pkrtz_f16_f32 v74, v176, v177
	v_fmac_f32_e32 v178, v112, v177
	v_pk_mul_f16 v74, v58, v74
	s_waitcnt lgkmcnt(2)
	v_add_f32_e32 v196, v85, v90
	v_fmac_f32_e32 v179, v113, v178
	v_add_f32_e32 v88, v84, v89
	v_cvt_pkrtz_f16_f32 v75, v178, v179
	v_pk_mul_f16 v75, v59, v75
	v_exp_f32_e32 v114, v114
	v_exp_f32_e32 v115, v115
	v_mfma_f32_16x16x32_f16 v[76:79], v[72:75], v[24:27], v[76:79]
	ds_read_b128 v[52:55], v92 offset:40960
	ds_bpermute_b32 v90, v87, v88
	s_waitcnt lgkmcnt(2)
	v_exp_f32_e32 v116, v116
	v_exp_f32_e32 v117, v117
	v_mfma_f32_32x32x8_f16 v[98:113], v[32:33], v[28:29], 0
	ds_read_u16 v32, v9 offset:160
	ds_read_b128 v[56:59], v92 offset:41984
	v_fmac_f32_e32 v148, v114, v179
	v_exp_f32_e32 v118, v118
	v_fmac_f32_e32 v149, v115, v148
	v_exp_f32_e32 v119, v119
	v_fmac_f32_e32 v150, v116, v149
	v_cvt_pkrtz_f16_f32 v68, v148, v149
	v_exp_f32_e32 v120, v120
	v_fmac_f32_e32 v151, v117, v150
	v_pk_mul_f16 v68, v60, v68
	v_exp_f32_e32 v121, v121
	v_add_f32_e32 v84, v76, v77
	v_add_f32_e32 v91, v78, v79
	v_fmac_f32_e32 v152, v118, v151
	v_add_f32_e32 v84, v84, v91
	v_cvt_pkrtz_f16_f32 v69, v150, v151
	v_mfma_f32_32x32x16_f16 v[132:147], v[36:39], v[44:47], 0
	ds_read_b128 v[44:47], v92 offset:10240
	ds_bpermute_b32 v89, v86, v84
	v_exp_f32_e32 v122, v122
	v_fmac_f32_e32 v153, v119, v152
	v_pk_mul_f16 v69, v61, v69
	v_exp_f32_e32 v123, v123
	v_fmac_f32_e32 v154, v120, v153
	v_cvt_pkrtz_f16_f32 v70, v152, v153
	v_exp_f32_e32 v124, v124
	v_fmac_f32_e32 v155, v121, v154
	v_pk_mul_f16 v70, v62, v70
	v_exp_f32_e32 v125, v125
	v_mfma_f32_32x32x16_f16 v[164:179], v[36:39], v[48:51], 0
	ds_read_b128 v[36:39], v11 offset:1280
	ds_read_b128 v[48:51], v92 offset:11264
	v_cvt_pkrtz_f16_f32 v71, v154, v155
	v_fmac_f32_e32 v188, v122, v155
	v_pk_mul_f16 v71, v63, v71
	v_exp_f32_e32 v126, v126
	v_fmac_f32_e32 v189, v123, v188
	v_mfma_f32_16x16x32_f16 v[80:83], v[68:71], v[20:23], 0
	v_cvt_pkrtz_f16_f32 v72, v188, v189
	v_exp_f32_e32 v127, v127
	v_fmac_f32_e32 v190, v124, v189
	v_pk_mul_f16 v72, v64, v72
	v_fmac_f32_e32 v191, v125, v190
	v_exp_f32_e32 v128, v128
	v_cvt_pkrtz_f16_f32 v73, v190, v191
	v_fmac_f32_e32 v192, v126, v191
	v_pk_mul_f16 v73, v65, v73
	v_fmac_f32_e32 v193, v127, v192
	v_exp_f32_e32 v129, v129
	v_cvt_pkrtz_f16_f32 v74, v192, v193
	v_fmac_f32_e32 v194, v128, v193
	v_pk_mul_f16 v74, v66, v74
	s_waitcnt lgkmcnt(2)
	v_add_f32_e32 v197, v88, v90
	v_fmac_f32_e32 v195, v129, v194
	v_add_f32_e32 v85, v84, v89
	v_cvt_pkrtz_f16_f32 v75, v194, v195
	v_pk_mul_f16 v75, v67, v75
	v_exp_f32_e32 v98, v98
	v_exp_f32_e32 v99, v99
	v_mfma_f32_16x16x32_f16 v[80:83], v[72:75], v[24:27], v[80:83]
	ds_read_b128 v[60:63], v92 offset:43008
	ds_bpermute_b32 v90, v87, v85
	s_waitcnt lgkmcnt(2)
	v_exp_f32_e32 v100, v100
	v_exp_f32_e32 v101, v101
	v_mfma_f32_32x32x8_f16 v[114:129], v[32:33], v[28:29], 0
	ds_read_u16 v32, v9 offset:192
	ds_read_b128 v[64:67], v92 offset:44032
	v_fmac_f32_e32 v132, v98, v195
	v_exp_f32_e32 v102, v102
	v_fmac_f32_e32 v133, v99, v132
	v_exp_f32_e32 v103, v103
	v_fmac_f32_e32 v134, v100, v133
	v_cvt_pkrtz_f16_f32 v68, v132, v133
	v_exp_f32_e32 v104, v104
	v_fmac_f32_e32 v135, v101, v134
	v_pk_mul_f16 v68, v52, v68
	v_exp_f32_e32 v105, v105
	v_add_f32_e32 v84, v80, v81
	v_add_f32_e32 v91, v82, v83
	v_fmac_f32_e32 v136, v102, v135
	v_add_f32_e32 v84, v84, v91
	v_cvt_pkrtz_f16_f32 v69, v134, v135
	v_mfma_f32_32x32x16_f16 v[148:163], v[36:39], v[44:47], 0
	ds_read_b128 v[44:47], v92 offset:12288
	ds_bpermute_b32 v89, v86, v84
	v_exp_f32_e32 v106, v106
	v_fmac_f32_e32 v137, v103, v136
	v_pk_mul_f16 v69, v53, v69
	v_exp_f32_e32 v107, v107
	v_fmac_f32_e32 v138, v104, v137
	v_cvt_pkrtz_f16_f32 v70, v136, v137
	v_exp_f32_e32 v108, v108
	v_fmac_f32_e32 v139, v105, v138
	v_pk_mul_f16 v70, v54, v70
	v_exp_f32_e32 v109, v109
	v_mfma_f32_32x32x16_f16 v[180:195], v[36:39], v[48:51], 0
	ds_read_b128 v[36:39], v11 offset:1536
	ds_read_b128 v[48:51], v92 offset:13312
	v_cvt_pkrtz_f16_f32 v71, v138, v139
	v_fmac_f32_e32 v172, v106, v139
	v_pk_mul_f16 v71, v55, v71
	v_exp_f32_e32 v110, v110
	v_fmac_f32_e32 v173, v107, v172
	v_mfma_f32_16x16x32_f16 v[76:79], v[68:71], v[20:23], 0
	v_cvt_pkrtz_f16_f32 v72, v172, v173
	v_exp_f32_e32 v111, v111
	v_fmac_f32_e32 v174, v108, v173
	v_pk_mul_f16 v72, v56, v72
	v_fmac_f32_e32 v175, v109, v174
	v_exp_f32_e32 v112, v112
	v_cvt_pkrtz_f16_f32 v73, v174, v175
	v_fmac_f32_e32 v176, v110, v175
	v_pk_mul_f16 v73, v57, v73
	v_fmac_f32_e32 v177, v111, v176
	v_exp_f32_e32 v113, v113
	v_cvt_pkrtz_f16_f32 v74, v176, v177
	v_fmac_f32_e32 v178, v112, v177
	v_pk_mul_f16 v74, v58, v74
	s_waitcnt lgkmcnt(2)
	v_add_f32_e32 v198, v85, v90
	v_fmac_f32_e32 v179, v113, v178
	v_add_f32_e32 v88, v84, v89
	v_cvt_pkrtz_f16_f32 v75, v178, v179
	v_pk_mul_f16 v75, v59, v75
	v_exp_f32_e32 v114, v114
	v_exp_f32_e32 v115, v115
	v_mfma_f32_16x16x32_f16 v[76:79], v[72:75], v[24:27], v[76:79]
	ds_read_b128 v[52:55], v92 offset:45056
	ds_bpermute_b32 v90, v87, v88
	s_waitcnt lgkmcnt(2)
	s_waitcnt vmcnt(0)
	ds_write_b16 v94, v18
	ds_write_b16 v94, v19 offset:1024
	ds_read_b128 v[204:207], v92 offset:47104
	ds_read_b128 v[208:211], v92 offset:48128
	v_exp_f32_e32 v116, v116
	v_exp_f32_e32 v117, v117
	v_mfma_f32_32x32x8_f16 v[98:113], v[32:33], v[28:29], 0
	ds_read_u16 v32, v9 offset:224
	ds_read_b128 v[56:59], v92 offset:46080
	v_fmac_f32_e32 v148, v114, v179
	v_exp_f32_e32 v118, v118
	v_fmac_f32_e32 v149, v115, v148
	v_exp_f32_e32 v119, v119
	v_fmac_f32_e32 v150, v116, v149
	v_cvt_pkrtz_f16_f32 v68, v148, v149
	v_exp_f32_e32 v120, v120
	v_fmac_f32_e32 v151, v117, v150
	v_pk_mul_f16 v68, v60, v68
	v_exp_f32_e32 v121, v121
	v_add_f32_e32 v84, v76, v77
	v_add_f32_e32 v91, v78, v79
	v_fmac_f32_e32 v152, v118, v151
	v_add_f32_e32 v84, v84, v91
	v_cvt_pkrtz_f16_f32 v69, v150, v151
	v_mfma_f32_32x32x16_f16 v[132:147], v[36:39], v[44:47], 0
	ds_read_b128 v[44:47], v92 offset:14336
	ds_bpermute_b32 v89, v86, v84
	v_exp_f32_e32 v122, v122
	v_fmac_f32_e32 v153, v119, v152
	v_pk_mul_f16 v69, v61, v69
	v_exp_f32_e32 v123, v123
	v_fmac_f32_e32 v154, v120, v153
	v_cvt_pkrtz_f16_f32 v70, v152, v153
	v_exp_f32_e32 v124, v124
	v_fmac_f32_e32 v155, v121, v154
	v_pk_mul_f16 v70, v62, v70
	v_exp_f32_e32 v125, v125
	v_mfma_f32_32x32x16_f16 v[164:179], v[36:39], v[48:51], 0
	ds_read_b128 v[36:39], v11 offset:1792
	ds_read_b128 v[48:51], v92 offset:15360
	v_cvt_pkrtz_f16_f32 v71, v154, v155
	v_fmac_f32_e32 v188, v122, v155
	v_pk_mul_f16 v71, v63, v71
	v_exp_f32_e32 v126, v126
	v_fmac_f32_e32 v189, v123, v188
	v_mfma_f32_16x16x32_f16 v[80:83], v[68:71], v[20:23], 0
	v_cvt_pkrtz_f16_f32 v72, v188, v189
	v_exp_f32_e32 v127, v127
	v_fmac_f32_e32 v190, v124, v189
	v_pk_mul_f16 v72, v64, v72
	v_fmac_f32_e32 v191, v125, v190
	v_exp_f32_e32 v128, v128
	v_cvt_pkrtz_f16_f32 v73, v190, v191
	v_fmac_f32_e32 v192, v126, v191
	v_pk_mul_f16 v73, v65, v73
	v_fmac_f32_e32 v193, v127, v192
	v_exp_f32_e32 v129, v129
	v_cvt_pkrtz_f16_f32 v74, v192, v193
	v_fmac_f32_e32 v194, v128, v193
	v_pk_mul_f16 v74, v66, v74
	s_waitcnt lgkmcnt(2)
	v_add_f32_e32 v199, v88, v90
	v_fmac_f32_e32 v195, v129, v194
	v_add_f32_e32 v85, v84, v89
	v_cvt_pkrtz_f16_f32 v75, v194, v195
	v_pk_mul_f16 v75, v67, v75
	v_exp_f32_e32 v98, v98
	v_exp_f32_e32 v99, v99
	v_mfma_f32_16x16x32_f16 v[80:83], v[72:75], v[24:27], v[80:83]
	s_waitcnt lgkmcnt(0)
	s_barrier
	ds_bpermute_b32 v90, v87, v85
	v_exp_f32_e32 v100, v100
	v_exp_f32_e32 v101, v101
	v_mfma_f32_32x32x8_f16 v[114:129], v[32:33], v[28:29], 0
	s_mov_b32 m0, s32
	ds_read_u16 v32, v10 offset:0
	global_load_lds_dwordx4 v2, s[20:21]
	v_fmac_f32_e32 v132, v98, v195
	v_exp_f32_e32 v102, v102
	v_fmac_f32_e32 v133, v99, v132
	v_exp_f32_e32 v103, v103
	v_fmac_f32_e32 v134, v100, v133
	v_cvt_pkrtz_f16_f32 v68, v132, v133
	v_exp_f32_e32 v104, v104
	v_fmac_f32_e32 v135, v101, v134
	v_pk_mul_f16 v68, v52, v68
	v_exp_f32_e32 v105, v105
	v_add_f32_e32 v84, v80, v81
	v_add_f32_e32 v91, v82, v83
	v_fmac_f32_e32 v136, v102, v135
	v_add_f32_e32 v84, v84, v91
	v_cvt_pkrtz_f16_f32 v69, v134, v135
	v_mfma_f32_32x32x16_f16 v[148:163], v[36:39], v[44:47], 0
	ds_read_b128 v[44:47], v93 offset:0
	ds_bpermute_b32 v89, v86, v84
	s_add_i32 m0, s32, 32768
	s_nop 0
	global_load_lds_dwordx4 v2, s[22:23]
	v_exp_f32_e32 v106, v106
	v_fmac_f32_e32 v137, v103, v136
	v_pk_mul_f16 v69, v53, v69
	v_exp_f32_e32 v107, v107
	v_fmac_f32_e32 v138, v104, v137
	v_cvt_pkrtz_f16_f32 v70, v136, v137
	v_exp_f32_e32 v108, v108
	v_fmac_f32_e32 v139, v105, v138
	v_pk_mul_f16 v70, v54, v70
	v_exp_f32_e32 v109, v109
	v_mfma_f32_32x32x16_f16 v[180:195], v[36:39], v[48:51], 0
	ds_read_b128 v[36:39], v13 offset:0
	s_mov_b32 m0, s33
	ds_read_b128 v[48:51], v93 offset:1024
	global_load_lds_dwordx4 v3, s[20:21]
	v_cvt_pkrtz_f16_f32 v71, v138, v139
	v_fmac_f32_e32 v172, v106, v139
	v_pk_mul_f16 v71, v55, v71
	v_exp_f32_e32 v110, v110
	v_fmac_f32_e32 v173, v107, v172
	v_mfma_f32_16x16x32_f16 v[76:79], v[68:71], v[20:23], 0
	s_add_i32 m0, s33, 32768
	s_nop 0
	global_load_lds_dwordx4 v3, s[22:23]
	v_cvt_pkrtz_f16_f32 v72, v172, v173
	v_exp_f32_e32 v111, v111
	v_fmac_f32_e32 v174, v108, v173
	v_pk_mul_f16 v72, v56, v72
	v_fmac_f32_e32 v175, v109, v174
	v_exp_f32_e32 v112, v112
	v_cvt_pkrtz_f16_f32 v73, v174, v175
	v_fmac_f32_e32 v176, v110, v175
	v_pk_mul_f16 v73, v57, v73
	v_fmac_f32_e32 v177, v111, v176
	v_exp_f32_e32 v113, v113
	v_cvt_pkrtz_f16_f32 v74, v176, v177
	v_fmac_f32_e32 v178, v112, v177
	v_pk_mul_f16 v74, v58, v74
	s_waitcnt lgkmcnt(2)
	v_add_f32_e32 v200, v85, v90
	v_fmac_f32_e32 v179, v113, v178
	v_add_f32_e32 v88, v84, v89
	v_cvt_pkrtz_f16_f32 v75, v178, v179
	v_pk_mul_f16 v75, v59, v75
	v_exp_f32_e32 v114, v114
	v_exp_f32_e32 v115, v115
	v_mfma_f32_16x16x32_f16 v[76:79], v[72:75], v[24:27], v[76:79]
	s_mov_b32 m0, s34
	ds_read_b128 v[52:55], v93 offset:32768
	global_load_lds_dwordx4 v4, s[20:21]
	ds_bpermute_b32 v90, v87, v88
	s_waitcnt lgkmcnt(2)
	v_exp_f32_e32 v116, v116
	v_exp_f32_e32 v117, v117
	v_mfma_f32_32x32x8_f16 v[98:113], v[32:33], v[28:29], 0
	ds_read_u16 v32, v10 offset:32
	s_add_i32 m0, s34, 32768
	ds_read_b128 v[56:59], v93 offset:33792
	global_load_lds_dwordx4 v4, s[22:23]
	v_fmac_f32_e32 v148, v114, v179
	v_exp_f32_e32 v118, v118
	v_fmac_f32_e32 v149, v115, v148
	v_exp_f32_e32 v119, v119
	v_fmac_f32_e32 v150, v116, v149
	v_cvt_pkrtz_f16_f32 v68, v148, v149
	v_exp_f32_e32 v120, v120
	v_fmac_f32_e32 v151, v117, v150
	v_pk_mul_f16 v68, v204, v68
	v_exp_f32_e32 v121, v121
	v_add_f32_e32 v84, v76, v77
	v_add_f32_e32 v91, v78, v79
	v_fmac_f32_e32 v152, v118, v151
	v_add_f32_e32 v84, v84, v91
	v_cvt_pkrtz_f16_f32 v69, v150, v151
	v_mfma_f32_32x32x16_f16 v[132:147], v[36:39], v[44:47], 0
	ds_read_b128 v[44:47], v93 offset:2048
	ds_bpermute_b32 v89, v86, v84
	s_cmp_eq_u32 s40, 0
	s_cselect_b64 s[56:57], 0, s[42:43]
	s_and_saveexec_b64 s[44:45], s[56:57]
	global_store_dword v[16:17], v201, off offset:-192 sc1
	global_store_dword v[16:17], v202, off offset:-128 sc1
	global_store_dword v[16:17], v203, off offset:-64 sc1
	s_and_b64 exec, s[44:45], s[42:43]
	global_store_dword v[16:17], v196, off sc1
	global_store_dword v[16:17], v197, off offset:64 sc1
	global_store_dword v[16:17], v198, off offset:128 sc1
	global_store_dword v[16:17], v199, off offset:192 sc1
	global_store_dword v[16:17], v200, off offset:256 sc1
	s_mov_b64 exec, s[44:45]
	v_exp_f32_e32 v122, v122
	v_fmac_f32_e32 v153, v119, v152
	v_pk_mul_f16 v69, v205, v69
	v_exp_f32_e32 v123, v123
	v_fmac_f32_e32 v154, v120, v153
	v_cvt_pkrtz_f16_f32 v70, v152, v153
	v_exp_f32_e32 v124, v124
	v_fmac_f32_e32 v155, v121, v154
	v_pk_mul_f16 v70, v206, v70
	v_exp_f32_e32 v125, v125
	v_mfma_f32_32x32x16_f16 v[164:179], v[36:39], v[48:51], 0
	ds_read_b128 v[36:39], v13 offset:256
	s_mov_b32 m0, s35
	ds_read_b128 v[48:51], v93 offset:3072
	global_load_lds_dwordx4 v5, s[20:21]
	s_add_i32 m0, s35, 32768
	s_nop 0
	global_load_lds_dwordx4 v5, s[22:23]
	v_cvt_pkrtz_f16_f32 v71, v154, v155
	v_fmac_f32_e32 v188, v122, v155
	v_pk_mul_f16 v71, v207, v71
	v_exp_f32_e32 v126, v126
	v_fmac_f32_e32 v189, v123, v188
	v_mfma_f32_16x16x32_f16 v[80:83], v[68:71], v[20:23], 0
	s_mov_b32 m0, s29
	s_nop 0
	global_load_lds_dword v6, s[24:25]
	global_load_ushort v18, v7, s[26:27]
	global_load_ushort v19, v7, s[26:27] offset:128
	v_cvt_pkrtz_f16_f32 v72, v188, v189
	v_exp_f32_e32 v127, v127
	v_fmac_f32_e32 v190, v124, v189
	v_pk_mul_f16 v72, v208, v72
	v_fmac_f32_e32 v191, v125, v190
	v_exp_f32_e32 v128, v128
	v_cvt_pkrtz_f16_f32 v73, v190, v191
	v_fmac_f32_e32 v192, v126, v191
	v_pk_mul_f16 v73, v209, v73
	v_fmac_f32_e32 v193, v127, v192
	v_exp_f32_e32 v129, v129
	v_cvt_pkrtz_f16_f32 v74, v192, v193
	v_fmac_f32_e32 v194, v128, v193
	v_pk_mul_f16 v74, v210, v74
	s_waitcnt lgkmcnt(2)
	v_add_f32_e32 v201, v88, v90
	v_fmac_f32_e32 v195, v129, v194
	v_add_f32_e32 v85, v84, v89
	v_cvt_pkrtz_f16_f32 v75, v194, v195
	s_cmp_lt_u32 s40, 29
	s_cselect_b32 s58, 0x4000, 0
	s_cselect_b32 s59, 0x100, 0
	s_add_u32 s20, s20, s58
	s_addc_u32 s21, s21, 0
	s_add_u32 s22, s22, s58
	s_addc_u32 s23, s23, 0
	s_add_u32 s24, s24, s59
	s_addc_u32 s25, s25, 0
	s_add_u32 s26, s26, s59
	s_addc_u32 s27, s27, 0
	v_pk_mul_f16 v75, v211, v75
	v_lshl_add_u64 v[16:17], v[16:17], 0, s[46:47]
	v_swap_b32 v92, v93
	v_swap_b32 v9, v10
	v_swap_b32 v11, v13
	v_swap_b32 v8, v94
	s_xor_b32 s32, s32, 0x4000
	s_xor_b32 s33, s33, 0x4000
	s_xor_b32 s34, s34, 0x4000
	s_xor_b32 s35, s35, 0x4000
	s_xor_b32 s29, s29, 0x100
	s_add_u32 s40, s40, 1
	s_cmp_lt_u32 s40, 32
	s_cbranch_scc1 .Lscan_loop
	s_nop 1
	v_mfma_f32_16x16x32_f16 v[80:83], v[72:75], v[24:27], v[80:83]
	ds_bpermute_b32 v90, v87, v85
	s_nop 15
	v_add_f32_e32 v84, v80, v81
	v_add_f32_e32 v91, v82, v83
	s_nop 0
	v_add_f32_e32 v84, v84, v91
	s_waitcnt lgkmcnt(0)
	v_add_f32_e32 v202, v85, v90
	ds_bpermute_b32 v89, v86, v84
	s_waitcnt lgkmcnt(0)
	v_add_f32_e32 v88, v84, v89
	s_nop 0
	ds_bpermute_b32 v90, v87, v88
	s_waitcnt lgkmcnt(0)
	v_add_f32_e32 v203, v88, v90
	s_nop 1
	s_and_saveexec_b64 s[44:45], s[42:43]
	global_store_dword v[16:17], v201, off offset:-192 sc1
	global_store_dword v[16:17], v202, off offset:-128 sc1
	global_store_dword v[16:17], v203, off offset:-64 sc1
	s_waitcnt vmcnt(0)
	s_endpgm

	.amdhsa_kernel _Z6scan_kPKDF16_S0_S0_S0_PKfPf
		.amdhsa_group_segment_fixed_size 86016
		.amdhsa_private_segment_fixed_size 0
		.amdhsa_kernarg_size 48
		.amdhsa_user_sgpr_count 2
		.amdhsa_user_sgpr_dispatch_ptr 0
		.amdhsa_user_sgpr_queue_ptr 0
		.amdhsa_user_sgpr_kernarg_segment_ptr 1
		.amdhsa_user_sgpr_dispatch_id 0
		.amdhsa_user_sgpr_kernarg_preload_length 0
		.amdhsa_user_sgpr_kernarg_preload_offset 0
		.amdhsa_user_sgpr_private_segment_size 0
		.amdhsa_uses_dynamic_stack 0
		.amdhsa_enable_private_segment 0
		.amdhsa_system_sgpr_workgroup_id_x 1
		.amdhsa_system_sgpr_workgroup_id_y 0
		.amdhsa_system_sgpr_workgroup_id_z 0
		.amdhsa_system_sgpr_workgroup_info 0
		.amdhsa_system_vgpr_workitem_id 0
		.amdhsa_next_free_vgpr 212
		.amdhsa_next_free_sgpr 96
		.amdhsa_accum_offset 212
		.amdhsa_reserve_vcc 1
		.amdhsa_float_round_mode_32 0
		.amdhsa_float_round_mode_16_64 0
		.amdhsa_float_denorm_mode_32 3
		.amdhsa_float_denorm_mode_16_64 3
		.amdhsa_dx10_clamp 1
		.amdhsa_ieee_mode 1
		.amdhsa_fp16_overflow 0
		.amdhsa_tg_split 0
		.amdhsa_exception_fp_ieee_invalid_op 0
		.amdhsa_exception_fp_denorm_src 0
		.amdhsa_exception_fp_ieee_div_zero 0
		.amdhsa_exception_fp_ieee_overflow 0
		.amdhsa_exception_fp_ieee_underflow 0
		.amdhsa_exception_fp_ieee_inexact 0
		.amdhsa_exception_int_div_zero 0
	.end_amdhsa_kernel

.LBB11_10:
	s_mul_i32 s7, s26, 0x6000
	v_add_u32_e32 v36, s7, v18
	v_add_u32_e32 v37, s7, v20
	v_add_u32_e32 v24, v36, v19
	v_add_u32_e32 v28, v37, v19
	v_add_u32_e32 v25, v36, v21
	v_add_u32_e32 v29, v37, v21
	ds_read_b128 v[40:43], v24
	ds_read_b128 v[56:59], v28 offset:8192
	ds_read_b128 v[72:75], v28 offset:12288
	v_add_u32_e32 v26, v36, v22
	v_add_u32_e32 v30, v37, v22
	ds_read_b128 v[44:47], v25
	ds_read_b128 v[60:63], v29 offset:8192
	ds_read_b128 v[76:79], v29 offset:12288
	v_add_u32_e32 v27, v36, v23
	v_add_u32_e32 v31, v37, v23
	ds_read_b128 v[48:51], v26
	ds_read_b128 v[64:67], v30 offset:8192
	ds_read_b128 v[80:83], v30 offset:12288
	ds_read_b128 v[52:55], v27
	ds_read_b128 v[68:71], v31 offset:8192
	ds_read_b128 v[84:87], v31 offset:12288
	s_add_i32 s7, s26, 1
	s_cmp_lg_u32 s26, 2
	s_cselect_b32 s26, s7, 0
	s_add_i32 s7, s25, 1
	s_cmp_lg_u32 s25, 2
	s_cselect_b32 s25, s7, 0
	s_add_i32 s27, s27, 1
	s_cmp_eq_u32 s12, s27
	s_waitcnt lgkmcnt(9)
	v_mfma_f32_16x16x32_f16 a[0:3], v[40:43], v[56:59], a[0:3]
	v_mfma_f32_16x16x32_f16 a[4:7], v[40:43], v[72:75], a[4:7]
	s_waitcnt lgkmcnt(6)
	v_mfma_f32_16x16x32_f16 a[0:3], v[44:47], v[60:63], a[0:3]
	v_mfma_f32_16x16x32_f16 a[4:7], v[44:47], v[76:79], a[4:7]
	s_waitcnt lgkmcnt(3)
	v_mfma_f32_16x16x32_f16 a[0:3], v[48:51], v[64:67], a[0:3]
	v_mfma_f32_16x16x32_f16 a[4:7], v[48:51], v[80:83], a[4:7]
	s_waitcnt lgkmcnt(0)
	v_mfma_f32_16x16x32_f16 a[0:3], v[52:55], v[68:71], a[0:3]
	v_mfma_f32_16x16x32_f16 a[4:7], v[52:55], v[84:87], a[4:7]
	s_cbranch_scc1 .LBB11_18

	.amdhsa_kernel _Z6gemm_gILi32ELi64ELi16ELi32ELi1ELi1ELi128ELi3EEv5GemmP
		.amdhsa_group_segment_fixed_size 73728
		.amdhsa_private_segment_fixed_size 0
		.amdhsa_kernarg_size 112
		.amdhsa_user_sgpr_count 2
		.amdhsa_user_sgpr_dispatch_ptr 0
		.amdhsa_user_sgpr_queue_ptr 0
		.amdhsa_user_sgpr_kernarg_segment_ptr 1
		.amdhsa_user_sgpr_dispatch_id 0
		.amdhsa_user_sgpr_kernarg_preload_length 0
		.amdhsa_user_sgpr_kernarg_preload_offset 0
		.amdhsa_user_sgpr_private_segment_size 0
		.amdhsa_uses_dynamic_stack 0
		.amdhsa_enable_private_segment 0
		.amdhsa_system_sgpr_workgroup_id_x 1
		.amdhsa_system_sgpr_workgroup_id_y 1
		.amdhsa_system_sgpr_workgroup_id_z 0
		.amdhsa_system_sgpr_workgroup_info 0
		.amdhsa_system_vgpr_workitem_id 0
		.amdhsa_next_free_vgpr 169
		.amdhsa_next_free_sgpr 96
		.amdhsa_accum_offset 88
		.amdhsa_reserve_vcc 1
		.amdhsa_float_round_mode_32 0
		.amdhsa_float_round_mode_16_64 0
		.amdhsa_float_denorm_mode_32 3
		.amdhsa_float_denorm_mode_16_64 3
		.amdhsa_dx10_clamp 1
		.amdhsa_ieee_mode 1
		.amdhsa_fp16_overflow 0
		.amdhsa_tg_split 0
		.amdhsa_exception_fp_ieee_invalid_op 0
		.amdhsa_exception_fp_denorm_src 0
		.amdhsa_exception_fp_ieee_div_zero 0
		.amdhsa_exception_fp_ieee_overflow 0
		.amdhsa_exception_fp_ieee_underflow 0
		.amdhsa_exception_fp_ieee_inexact 0
		.amdhsa_exception_int_div_zero 0
	.end_amdhsa_kernel

amdhsa.kernels:
  - .agpr_count:     0
    .args:
      - .offset:         0
        .size:           152
        .value_kind:     by_value
    .group_segment_fixed_size: 7168
    .kernarg_segment_align: 8
    .kernarg_segment_size: 152
    .language:       OpenCL C
    .language_version:
      - 2
      - 0
    .max_flat_workgroup_size: 256
    .name:           _Z6prep_k5PrepP
    .private_segment_fixed_size: 0
    .sgpr_count:     70
    .sgpr_spill_count: 0
    .symbol:         _Z6prep_k5PrepP.kd
    .uniform_work_group_size: 1
    .uses_dynamic_stack: false
    .vgpr_count:     64
    .vgpr_spill_count: 0
    .wavefront_size: 64
  - .agpr_count:     0
    .args:
      - .actual_access:  read_only
        .address_space:  global
        .offset:         0
        .size:           8
        .value_kind:     global_buffer
      - .actual_access:  read_only
        .address_space:  global
        .offset:         8
        .size:           8
        .value_kind:     global_buffer
      - .actual_access:  read_only
        .address_space:  global
        .offset:         16
        .size:           8
        .value_kind:     global_buffer
      - .actual_access:  write_only
        .address_space:  global
        .offset:         24
        .size:           8
        .value_kind:     global_buffer
      - .actual_access:  write_only
        .address_space:  global
        .offset:         32
        .size:           8
        .value_kind:     global_buffer
    .group_segment_fixed_size: 9216
    .kernarg_segment_align: 8
    .kernarg_segment_size: 40
    .language:       OpenCL C
    .language_version:
      - 2
      - 0
    .max_flat_workgroup_size: 256
    .name:           _Z8conv1d_kPKDF16_PKfS2_PDF16_S3_
    .private_segment_fixed_size: 0
    .sgpr_count:     22
    .sgpr_spill_count: 0
    .symbol:         _Z8conv1d_kPKDF16_PKfS2_PDF16_S3_.kd
    .uniform_work_group_size: 1
    .uses_dynamic_stack: false
    .vgpr_count:     53
    .vgpr_spill_count: 0
    .wavefront_size: 64
  - .agpr_count:     0
    .args:
      - .actual_access:  read_only
        .address_space:  global
        .offset:         0
        .size:           8
        .value_kind:     global_buffer
      - .actual_access:  read_only
        .address_space:  global
        .offset:         8
        .size:           8
        .value_kind:     global_buffer
      - .actual_access:  read_only
        .address_space:  global
        .offset:         16
        .size:           8
        .value_kind:     global_buffer
      - .actual_access:  read_only
        .address_space:  global
        .offset:         24
        .size:           8
        .value_kind:     global_buffer
      - .actual_access:  write_only
        .address_space:  global
        .offset:         32
        .size:           8
        .value_kind:     global_buffer
      - .actual_access:  write_only
        .address_space:  global
        .offset:         40
        .size:           8
        .value_kind:     global_buffer
    .group_segment_fixed_size: 70656
    .kernarg_segment_align: 8
    .kernarg_segment_size: 48
    .language:       OpenCL C
    .language_version:
      - 2
      - 0
    .max_flat_workgroup_size: 256
    .name:           _Z4dt_kPKfS0_S0_PKDF16_PDF16_S3_
    .private_segment_fixed_size: 0
    .sgpr_count:     25
    .sgpr_spill_count: 0
    .symbol:         _Z4dt_kPKfS0_S0_PKDF16_PDF16_S3_.kd
    .uniform_work_group_size: 1
    .uses_dynamic_stack: false
    .vgpr_count:     96
    .vgpr_spill_count: 0
    .wavefront_size: 64
  - .agpr_count:     0
    .args:
      - .address_space:  global
        .offset:         0
        .size:           8
        .value_kind:     global_buffer
      - .actual_access:  read_only
        .address_space:  global
        .offset:         8
        .size:           8
        .value_kind:     global_buffer
      - .address_space:  global
        .offset:         16
        .size:           8
        .value_kind:     global_buffer
      - .address_space:  global
        .offset:         24
        .size:           8
        .value_kind:     global_buffer
      - .actual_access:  read_only
        .address_space:  global
        .offset:         32
        .size:           8
        .value_kind:     global_buffer
      - .actual_access:  write_only
        .address_space:  global
        .offset:         40
        .size:           8
        .value_kind:     global_buffer
    .group_segment_fixed_size: 86016
    .kernarg_segment_align: 8
    .kernarg_segment_size: 48
    .language:       OpenCL C
    .language_version:
      - 2
      - 0
    .max_flat_workgroup_size: 256
    .name:           _Z6scan_kPKDF16_S0_S0_S0_PKfPf
    .private_segment_fixed_size: 0
    .sgpr_count:     66
    .sgpr_spill_count: 0
    .symbol:         _Z6scan_kPKDF16_S0_S0_S0_PKfPf.kd
    .uniform_work_group_size: 1
    .uses_dynamic_stack: false
    .vgpr_count:     212
    .vgpr_spill_count: 0
    .wavefront_size: 64
  - .agpr_count:     0
    .args:
      - .actual_access:  read_only
        .address_space:  global
        .offset:         0
        .size:           8
        .value_kind:     global_buffer
      - .actual_access:  read_only
        .address_space:  global
        .offset:         8
        .size:           8
        .value_kind:     global_buffer
      - .actual_access:  read_only
        .address_space:  global
        .offset:         16
        .size:           8
        .value_kind:     global_buffer
      - .actual_access:  read_only
        .address_space:  global
        .offset:         24
        .size:           8
        .value_kind:     global_buffer
      - .actual_access:  write_only
        .address_space:  global
        .offset:         32
        .size:           8
        .value_kind:     global_buffer
    .group_segment_fixed_size: 9216
    .kernarg_segment_align: 8
    .kernarg_segment_size: 40
    .language:       OpenCL C
    .language_version:
      - 2
      - 0
    .max_flat_workgroup_size: 256
    .name:           _Z6gate_kPKfPKDF16_S2_S0_PDF16_
    .private_segment_fixed_size: 0
    .sgpr_count:     22
    .sgpr_spill_count: 0
    .symbol:         _Z6gate_kPKfPKDF16_S2_S0_PDF16_.kd
    .uniform_work_group_size: 1
    .uses_dynamic_stack: false
    .vgpr_count:     46
    .vgpr_spill_count: 0
    .wavefront_size: 64
  - .agpr_count:     0
    .args:
      - .actual_access:  read_only
        .address_space:  global
        .offset:         0
        .size:           8
        .value_kind:     global_buffer
      - .actual_access:  read_only
        .address_space:  global
        .offset:         8
        .size:           8
        .value_kind:     global_buffer
      - .actual_access:  read_only
        .address_space:  global
        .offset:         16
        .size:           8
        .value_kind:     global_buffer
      - .actual_access:  write_only
        .address_space:  global
        .offset:         24
        .size:           8
        .value_kind:     global_buffer
    .group_segment_fixed_size: 43776
    .kernarg_segment_align: 8
    .kernarg_segment_size: 32
    .language:       OpenCL C
    .language_version:
      - 2
      - 0
    .max_flat_workgroup_size: 256
    .name:           _Z9deconv3_kPKDF16_PKfS2_Pf
    .private_segment_fixed_size: 0
    .sgpr_count:     30
    .sgpr_spill_count: 0
    .symbol:         _Z9deconv3_kPKDF16_PKfS2_Pf.kd
    .uniform_work_group_size: 1
    .uses_dynamic_stack: false
    .vgpr_count:     60
    .vgpr_spill_count: 0
    .wavefront_size: 64
  - .agpr_count:     8
    .args:
      - .offset:         0
        .size:           112
        .value_kind:     by_value
    .group_segment_fixed_size: 49152
    .kernarg_segment_align: 8
    .kernarg_segment_size: 112
    .language:       OpenCL C
    .language_version:
      - 2
      - 0
    .max_flat_workgroup_size: 256
    .name:           _Z6gemm_gILi32ELi64ELi16ELi32ELi1ELi0ELi64ELi4EEv5GemmP
    .private_segment_fixed_size: 0
    .sgpr_count:     34
    .sgpr_spill_count: 0
    .symbol:         _Z6gemm_gILi32ELi64ELi16ELi32ELi1ELi0ELi64ELi4EEv5GemmP.kd
    .uniform_work_group_size: 1
    .uses_dynamic_stack: false
    .vgpr_count:     40
    .vgpr_spill_count: 0
    .wavefront_size: 64
  - .agpr_count:     16
    .args:
      - .offset:         0
        .size:           112
        .value_kind:     by_value
    .group_segment_fixed_size: 65536
    .kernarg_segment_align: 8
    .kernarg_segment_size: 112
    .language:       OpenCL C
    .language_version:
      - 2
      - 0
    .max_flat_workgroup_size: 256
    .name:           _Z6gemm_gILi64ELi64ELi32ELi32ELi1ELi0ELi64ELi4EEv5GemmP
    .private_segment_fixed_size: 0
    .sgpr_count:     34
    .sgpr_spill_count: 0
    .symbol:         _Z6gemm_gILi64ELi64ELi32ELi32ELi1ELi0ELi64ELi4EEv5GemmP.kd
    .uniform_work_group_size: 1
    .uses_dynamic_stack: false
    .vgpr_count:     56
    .vgpr_spill_count: 0
    .wavefront_size: 64
  - .agpr_count:     32
    .args:
      - .offset:         0
        .size:           112
        .value_kind:     by_value
    .group_segment_fixed_size: 73728
    .kernarg_segment_align: 8
    .kernarg_segment_size: 112
    .language:       OpenCL C
    .language_version:
      - 2
      - 0
    .max_flat_workgroup_size: 256
    .name:           _Z6gemm_gILi64ELi128ELi32ELi64ELi0ELi2ELi64ELi3EEv5GemmP
    .private_segment_fixed_size: 0
    .sgpr_count:     27
    .sgpr_spill_count: 0
    .symbol:         _Z6gemm_gILi64ELi128ELi32ELi64ELi0ELi2ELi64ELi3EEv5GemmP.kd
    .uniform_work_group_size: 1
    .uses_dynamic_stack: false
    .vgpr_count:     80
    .vgpr_spill_count: 0
    .wavefront_size: 64
  - .agpr_count:     16
    .args:
      - .offset:         0
        .size:           112
        .value_kind:     by_value
    .group_segment_fixed_size: 49152
    .kernarg_segment_align: 8
    .kernarg_segment_size: 112
    .language:       OpenCL C
    .language_version:
      - 2
      - 0
    .max_flat_workgroup_size: 256
    .name:           _Z6gemm_gILi64ELi64ELi32ELi32ELi0ELi3ELi64ELi3EEv5GemmP
    .private_segment_fixed_size: 0
    .sgpr_count:     30
    .sgpr_spill_count: 0
    .symbol:         _Z6gemm_gILi64ELi64ELi32ELi32ELi0ELi3ELi64ELi3EEv5GemmP.kd
    .uniform_work_group_size: 1
    .uses_dynamic_stack: false
    .vgpr_count:     56
    .vgpr_spill_count: 0
    .wavefront_size: 64
  - .agpr_count:     16
    .args:
      - .offset:         0
        .size:           112
        .value_kind:     by_value
    .group_segment_fixed_size: 49152
    .kernarg_segment_align: 8
    .kernarg_segment_size: 112
    .language:       OpenCL C
    .language_version:
      - 2
      - 0
    .max_flat_workgroup_size: 256
    .name:           _Z6gemm_gILi64ELi64ELi32ELi32ELi0ELi4ELi64ELi3EEv5GemmP
    .private_segment_fixed_size: 0
    .sgpr_count:     27
    .sgpr_spill_count: 0
    .symbol:         _Z6gemm_gILi64ELi64ELi32ELi32ELi0ELi4ELi64ELi3EEv5GemmP.kd
    .uniform_work_group_size: 1
    .uses_dynamic_stack: false
    .vgpr_count:     52
    .vgpr_spill_count: 0
    .wavefront_size: 64
  - .agpr_count:     8
    .args:
      - .offset:         0
        .size:           112
        .value_kind:     by_value
    .group_segment_fixed_size: 73728
    .kernarg_segment_align: 8
    .kernarg_segment_size: 112
    .language:       OpenCL C
    .language_version:
      - 2
      - 0
    .max_flat_workgroup_size: 256
    .name:           _Z6gemm_gILi32ELi64ELi16ELi32ELi1ELi1ELi128ELi3EEv5GemmP
    .private_segment_fixed_size: 0
    .sgpr_count:     38
    .sgpr_spill_count: 0
    .symbol:         _Z6gemm_gILi32ELi64ELi16ELi32ELi1ELi1ELi128ELi3EEv5GemmP.kd
    .uniform_work_group_size: 1
    .uses_dynamic_stack: false
    .vgpr_count:     48
    .vgpr_spill_count: 0
    .wavefront_size: 64
  - .agpr_count:     0
    .args:
      - .offset:         0
        .size:           112
        .value_kind:     by_value
    .group_segment_fixed_size: 98304
    .kernarg_segment_align: 8
    .kernarg_segment_size: 112
    .language:       OpenCL C
    .language_version:
      - 2
      - 0
    .max_flat_workgroup_size: 256
    .name:           _Z6gemm_gILi32ELi64ELi16ELi32ELi1ELi1ELi64ELi4EEv5GemmP
    .private_segment_fixed_size: 0
    .sgpr_count:     36
    .sgpr_spill_count: 0
    .symbol:         _Z6gemm_gILi32ELi64ELi16ELi32ELi1ELi1ELi64ELi4EEv5GemmP.kd
    .uniform_work_group_size: 1
    .uses_dynamic_stack: false
    .vgpr_count:     148
    .vgpr_spill_count: 0
    .wavefront_size: 64
